# epilogue cleanups: 64-bit moves for the accumulator init, dropped two s_nop 15 that guarded no recent MFMA result
# speedup vs baseline: 1.0225x; 1.0043x over previous
.LBB0_1326:
	v_lshl_add_u32 v20, s50, 8, v167
	v_lshl_or_b32 v18, s51, 7, v201
	v_ashrrev_i32_e32 v21, 31, v20
	v_ashrrev_i32_e32 v19, 31, v18
	v_lshlrev_b64 v[16:17], 11, v[20:21]
	v_lshl_add_u64 v[16:17], s[4:5], 0, v[16:17]
	v_lshl_add_u64 v[16:17], v[16:17], 0, v[18:19]
	v_mbcnt_lo_u32_b32 v20, -1, 0
	v_mbcnt_hi_u32_b32 v20, -1, v20
	v_and_b32_e32 v20, 16, v20
	v_mov_b32_e32 v18, 0x8000
	v_cmp_eq_u32_e32 vcc, 0, v20
	s_nop 1
	v_cndmask_b32_e32 v18, -8, v18, vcc
	v_ashrrev_i32_e32 v19, 31, v18
	v_lshl_add_u64 v[16:17], v[16:17], 0, v[18:19]
	v_min_f32_e32 v132, s65, v132
	v_min_f32_e32 v133, s65, v133
	v_min_f32_e32 v134, s65, v134
	v_min_f32_e32 v135, s65, v135
	v_min_f32_e32 v124, s65, v124
	v_min_f32_e32 v125, s65, v125
	v_min_f32_e32 v126, s65, v126
	v_min_f32_e32 v127, s65, v127
	v_pk_mul_f32 v[0:1], v[132:133], s[62:63]
	v_pk_mul_f32 v[2:3], v[134:135], s[62:63]
	v_pk_mul_f32 v[4:5], v[124:125], s[62:63]
	v_pk_mul_f32 v[6:7], v[126:127], s[62:63]
	v_exp_f32_e32 v0, v0
	v_exp_f32_e32 v1, v1
	v_exp_f32_e32 v2, v2
	v_exp_f32_e32 v3, v3
	v_exp_f32_e32 v4, v4
	v_exp_f32_e32 v5, v5
	v_exp_f32_e32 v6, v6
	v_exp_f32_e32 v7, v7
	v_pk_add_f32 v[0:1], v[0:1], 1.0 op_sel_hi:[1,0]
	v_pk_add_f32 v[2:3], v[2:3], 1.0 op_sel_hi:[1,0]
	v_pk_add_f32 v[4:5], v[4:5], 1.0 op_sel_hi:[1,0]
	v_pk_add_f32 v[6:7], v[6:7], 1.0 op_sel_hi:[1,0]
	v_rcp_f32_e32 v0, v0
	v_rcp_f32_e32 v1, v1
	v_rcp_f32_e32 v2, v2
	v_rcp_f32_e32 v3, v3
	v_rcp_f32_e32 v4, v4
	v_rcp_f32_e32 v5, v5
	v_rcp_f32_e32 v6, v6
	v_rcp_f32_e32 v7, v7
	v_med3_f32 v128, v128, s42, v205
	v_med3_f32 v129, v129, s42, v205
	v_med3_f32 v130, v130, s42, v205
	v_med3_f32 v131, v131, s42, v205
	v_med3_f32 v120, v120, s42, v205
	v_med3_f32 v121, v121, s42, v205
	v_med3_f32 v122, v122, s42, v205
	v_med3_f32 v123, v123, s42, v205
	v_pk_mul_f32 v[0:1], v[0:1], v[132:133]
	v_pk_mul_f32 v[2:3], v[2:3], v[134:135]
	v_pk_mul_f32 v[4:5], v[4:5], v[124:125]
	v_pk_mul_f32 v[6:7], v[6:7], v[126:127]
	v_pk_mul_f32 v[0:1], v[0:1], v[128:129]
	v_pk_mul_f32 v[2:3], v[2:3], v[130:131]
	v_pk_mul_f32 v[4:5], v[4:5], v[120:121]
	v_pk_mul_f32 v[6:7], v[6:7], v[122:123]
	v_cvt_pk_fp8_f32 v220, v0, v1
	v_cvt_pk_fp8_f32 v221, v4, v5
	v_cvt_pk_fp8_f32 v220, v2, v3 op_sel:[0,0,1]
	v_cvt_pk_fp8_f32 v221, v6, v7 op_sel:[0,0,1]
	v_min_f32_e32 v148, s65, v148
	v_min_f32_e32 v149, s65, v149
	v_min_f32_e32 v150, s65, v150
	v_min_f32_e32 v151, s65, v151
	v_min_f32_e32 v140, s65, v140
	v_min_f32_e32 v141, s65, v141
	v_min_f32_e32 v142, s65, v142
	v_min_f32_e32 v143, s65, v143
	v_pk_mul_f32 v[8:9], v[148:149], s[62:63]
	v_pk_mul_f32 v[10:11], v[150:151], s[62:63]
	v_pk_mul_f32 v[12:13], v[140:141], s[62:63]
	v_pk_mul_f32 v[14:15], v[142:143], s[62:63]
	v_exp_f32_e32 v8, v8
	v_exp_f32_e32 v9, v9
	v_exp_f32_e32 v10, v10
	v_exp_f32_e32 v11, v11
	v_exp_f32_e32 v12, v12
	v_exp_f32_e32 v13, v13
	v_exp_f32_e32 v14, v14
	v_exp_f32_e32 v15, v15
	v_pk_add_f32 v[8:9], v[8:9], 1.0 op_sel_hi:[1,0]
	v_pk_add_f32 v[10:11], v[10:11], 1.0 op_sel_hi:[1,0]
	v_pk_add_f32 v[12:13], v[12:13], 1.0 op_sel_hi:[1,0]
	v_pk_add_f32 v[14:15], v[14:15], 1.0 op_sel_hi:[1,0]
	v_rcp_f32_e32 v8, v8
	v_rcp_f32_e32 v9, v9
	v_rcp_f32_e32 v10, v10
	v_rcp_f32_e32 v11, v11
	v_rcp_f32_e32 v12, v12
	v_rcp_f32_e32 v13, v13
	v_rcp_f32_e32 v14, v14
	v_rcp_f32_e32 v15, v15
	v_med3_f32 v144, v144, s42, v205
	v_med3_f32 v145, v145, s42, v205
	v_med3_f32 v146, v146, s42, v205
	v_med3_f32 v147, v147, s42, v205
	v_med3_f32 v136, v136, s42, v205
	v_med3_f32 v137, v137, s42, v205
	v_med3_f32 v138, v138, s42, v205
	v_med3_f32 v139, v139, s42, v205
	v_pk_mul_f32 v[8:9], v[8:9], v[148:149]
	v_pk_mul_f32 v[10:11], v[10:11], v[150:151]
	v_pk_mul_f32 v[12:13], v[12:13], v[140:141]
	v_pk_mul_f32 v[14:15], v[14:15], v[142:143]
	v_pk_mul_f32 v[8:9], v[8:9], v[144:145]
	v_pk_mul_f32 v[10:11], v[10:11], v[146:147]
	v_pk_mul_f32 v[12:13], v[12:13], v[136:137]
	v_pk_mul_f32 v[14:15], v[14:15], v[138:139]
	v_cvt_pk_fp8_f32 v222, v8, v9
	v_cvt_pk_fp8_f32 v223, v12, v13
	v_cvt_pk_fp8_f32 v222, v10, v11 op_sel:[0,0,1]
	v_cvt_pk_fp8_f32 v223, v14, v15 op_sel:[0,0,1]
	s_nop 1
	v_permlane16_swap_b32_e32 v220, v222
	v_permlane16_swap_b32_e32 v221, v223
	global_store_dwordx4 v[16:17], v[220:223], off
	v_lshl_add_u64 v[16:17], v[16:17], 0, s[58:59]
	v_min_f32_e32 v100, s65, v100
	v_min_f32_e32 v101, s65, v101
	v_min_f32_e32 v102, s65, v102
	v_min_f32_e32 v103, s65, v103
	v_min_f32_e32 v92, s65, v92
	v_min_f32_e32 v93, s65, v93
	v_min_f32_e32 v94, s65, v94
	v_min_f32_e32 v95, s65, v95
	v_pk_mul_f32 v[0:1], v[100:101], s[62:63]
	v_pk_mul_f32 v[2:3], v[102:103], s[62:63]
	v_pk_mul_f32 v[4:5], v[92:93], s[62:63]
	v_pk_mul_f32 v[6:7], v[94:95], s[62:63]
	v_exp_f32_e32 v0, v0
	v_exp_f32_e32 v1, v1
	v_exp_f32_e32 v2, v2
	v_exp_f32_e32 v3, v3
	v_exp_f32_e32 v4, v4
	v_exp_f32_e32 v5, v5
	v_exp_f32_e32 v6, v6
	v_exp_f32_e32 v7, v7
	v_pk_add_f32 v[0:1], v[0:1], 1.0 op_sel_hi:[1,0]
	v_pk_add_f32 v[2:3], v[2:3], 1.0 op_sel_hi:[1,0]
	v_pk_add_f32 v[4:5], v[4:5], 1.0 op_sel_hi:[1,0]
	v_pk_add_f32 v[6:7], v[6:7], 1.0 op_sel_hi:[1,0]
	v_rcp_f32_e32 v0, v0
	v_rcp_f32_e32 v1, v1
	v_rcp_f32_e32 v2, v2
	v_rcp_f32_e32 v3, v3
	v_rcp_f32_e32 v4, v4
	v_rcp_f32_e32 v5, v5
	v_rcp_f32_e32 v6, v6
	v_rcp_f32_e32 v7, v7
	v_med3_f32 v96, v96, s42, v205
	v_med3_f32 v97, v97, s42, v205
	v_med3_f32 v98, v98, s42, v205
	v_med3_f32 v99, v99, s42, v205
	v_med3_f32 v88, v88, s42, v205
	v_med3_f32 v89, v89, s42, v205
	v_med3_f32 v90, v90, s42, v205
	v_med3_f32 v91, v91, s42, v205
	v_pk_mul_f32 v[0:1], v[0:1], v[100:101]
	v_pk_mul_f32 v[2:3], v[2:3], v[102:103]
	v_pk_mul_f32 v[4:5], v[4:5], v[92:93]
	v_pk_mul_f32 v[6:7], v[6:7], v[94:95]
	v_pk_mul_f32 v[0:1], v[0:1], v[96:97]
	v_pk_mul_f32 v[2:3], v[2:3], v[98:99]
	v_pk_mul_f32 v[4:5], v[4:5], v[88:89]
	v_pk_mul_f32 v[6:7], v[6:7], v[90:91]
	v_cvt_pk_fp8_f32 v224, v0, v1
	v_cvt_pk_fp8_f32 v225, v4, v5
	v_cvt_pk_fp8_f32 v224, v2, v3 op_sel:[0,0,1]
	v_cvt_pk_fp8_f32 v225, v6, v7 op_sel:[0,0,1]
	v_min_f32_e32 v116, s65, v116
	v_min_f32_e32 v117, s65, v117
	v_min_f32_e32 v118, s65, v118
	v_min_f32_e32 v119, s65, v119
	v_min_f32_e32 v108, s65, v108
	v_min_f32_e32 v109, s65, v109
	v_min_f32_e32 v110, s65, v110
	v_min_f32_e32 v111, s65, v111
	v_pk_mul_f32 v[8:9], v[116:117], s[62:63]
	v_pk_mul_f32 v[10:11], v[118:119], s[62:63]
	v_pk_mul_f32 v[12:13], v[108:109], s[62:63]
	v_pk_mul_f32 v[14:15], v[110:111], s[62:63]
	v_exp_f32_e32 v8, v8
	v_exp_f32_e32 v9, v9
	v_exp_f32_e32 v10, v10
	v_exp_f32_e32 v11, v11
	v_exp_f32_e32 v12, v12
	v_exp_f32_e32 v13, v13
	v_exp_f32_e32 v14, v14
	v_exp_f32_e32 v15, v15
	v_pk_add_f32 v[8:9], v[8:9], 1.0 op_sel_hi:[1,0]
	v_pk_add_f32 v[10:11], v[10:11], 1.0 op_sel_hi:[1,0]
	v_pk_add_f32 v[12:13], v[12:13], 1.0 op_sel_hi:[1,0]
	v_pk_add_f32 v[14:15], v[14:15], 1.0 op_sel_hi:[1,0]
	v_rcp_f32_e32 v8, v8
	v_rcp_f32_e32 v9, v9
	v_rcp_f32_e32 v10, v10
	v_rcp_f32_e32 v11, v11
	v_rcp_f32_e32 v12, v12
	v_rcp_f32_e32 v13, v13
	v_rcp_f32_e32 v14, v14
	v_rcp_f32_e32 v15, v15
	v_med3_f32 v112, v112, s42, v205
	v_med3_f32 v113, v113, s42, v205
	v_med3_f32 v114, v114, s42, v205
	v_med3_f32 v115, v115, s42, v205
	v_med3_f32 v104, v104, s42, v205
	v_med3_f32 v105, v105, s42, v205
	v_med3_f32 v106, v106, s42, v205
	v_med3_f32 v107, v107, s42, v205
	v_pk_mul_f32 v[8:9], v[8:9], v[116:117]
	v_pk_mul_f32 v[10:11], v[10:11], v[118:119]
	v_pk_mul_f32 v[12:13], v[12:13], v[108:109]
	v_pk_mul_f32 v[14:15], v[14:15], v[110:111]
	v_pk_mul_f32 v[8:9], v[8:9], v[112:113]
	v_pk_mul_f32 v[10:11], v[10:11], v[114:115]
	v_pk_mul_f32 v[12:13], v[12:13], v[104:105]
	v_pk_mul_f32 v[14:15], v[14:15], v[106:107]
	v_cvt_pk_fp8_f32 v226, v8, v9
	v_cvt_pk_fp8_f32 v227, v12, v13
	v_cvt_pk_fp8_f32 v226, v10, v11 op_sel:[0,0,1]
	v_cvt_pk_fp8_f32 v227, v14, v15 op_sel:[0,0,1]
	s_nop 1
	v_permlane16_swap_b32_e32 v224, v226
	v_permlane16_swap_b32_e32 v225, v227
	global_store_dwordx4 v[16:17], v[224:227], off
	v_lshl_add_u64 v[16:17], v[16:17], 0, s[60:61]
	v_min_f32_e32 v68, s65, v68
	v_min_f32_e32 v69, s65, v69
	v_min_f32_e32 v70, s65, v70
	v_min_f32_e32 v71, s65, v71
	v_min_f32_e32 v60, s65, v60
	v_min_f32_e32 v61, s65, v61
	v_min_f32_e32 v62, s65, v62
	v_min_f32_e32 v63, s65, v63
	v_pk_mul_f32 v[0:1], v[68:69], s[62:63]
	v_pk_mul_f32 v[2:3], v[70:71], s[62:63]
	v_pk_mul_f32 v[4:5], v[60:61], s[62:63]
	v_pk_mul_f32 v[6:7], v[62:63], s[62:63]
	v_exp_f32_e32 v0, v0
	v_exp_f32_e32 v1, v1
	v_exp_f32_e32 v2, v2
	v_exp_f32_e32 v3, v3
	v_exp_f32_e32 v4, v4
	v_exp_f32_e32 v5, v5
	v_exp_f32_e32 v6, v6
	v_exp_f32_e32 v7, v7
	v_pk_add_f32 v[0:1], v[0:1], 1.0 op_sel_hi:[1,0]
	v_pk_add_f32 v[2:3], v[2:3], 1.0 op_sel_hi:[1,0]
	v_pk_add_f32 v[4:5], v[4:5], 1.0 op_sel_hi:[1,0]
	v_pk_add_f32 v[6:7], v[6:7], 1.0 op_sel_hi:[1,0]
	v_rcp_f32_e32 v0, v0
	v_rcp_f32_e32 v1, v1
	v_rcp_f32_e32 v2, v2
	v_rcp_f32_e32 v3, v3
	v_rcp_f32_e32 v4, v4
	v_rcp_f32_e32 v5, v5
	v_rcp_f32_e32 v6, v6
	v_rcp_f32_e32 v7, v7
	v_med3_f32 v64, v64, s42, v205
	v_med3_f32 v65, v65, s42, v205
	v_med3_f32 v66, v66, s42, v205
	v_med3_f32 v67, v67, s42, v205
	v_med3_f32 v56, v56, s42, v205
	v_med3_f32 v57, v57, s42, v205
	v_med3_f32 v58, v58, s42, v205
	v_med3_f32 v59, v59, s42, v205
	v_pk_mul_f32 v[0:1], v[0:1], v[68:69]
	v_pk_mul_f32 v[2:3], v[2:3], v[70:71]
	v_pk_mul_f32 v[4:5], v[4:5], v[60:61]
	v_pk_mul_f32 v[6:7], v[6:7], v[62:63]
	v_pk_mul_f32 v[0:1], v[0:1], v[64:65]
	v_pk_mul_f32 v[2:3], v[2:3], v[66:67]
	v_pk_mul_f32 v[4:5], v[4:5], v[56:57]
	v_pk_mul_f32 v[6:7], v[6:7], v[58:59]
	v_cvt_pk_fp8_f32 v220, v0, v1
	v_cvt_pk_fp8_f32 v221, v4, v5
	v_cvt_pk_fp8_f32 v220, v2, v3 op_sel:[0,0,1]
	v_cvt_pk_fp8_f32 v221, v6, v7 op_sel:[0,0,1]
	v_min_f32_e32 v84, s65, v84
	v_min_f32_e32 v85, s65, v85
	v_min_f32_e32 v86, s65, v86
	v_min_f32_e32 v87, s65, v87
	v_min_f32_e32 v76, s65, v76
	v_min_f32_e32 v77, s65, v77
	v_min_f32_e32 v78, s65, v78
	v_min_f32_e32 v79, s65, v79
	v_pk_mul_f32 v[8:9], v[84:85], s[62:63]
	v_pk_mul_f32 v[10:11], v[86:87], s[62:63]
	v_pk_mul_f32 v[12:13], v[76:77], s[62:63]
	v_pk_mul_f32 v[14:15], v[78:79], s[62:63]
	v_exp_f32_e32 v8, v8
	v_exp_f32_e32 v9, v9
	v_exp_f32_e32 v10, v10
	v_exp_f32_e32 v11, v11
	v_exp_f32_e32 v12, v12
	v_exp_f32_e32 v13, v13
	v_exp_f32_e32 v14, v14
	v_exp_f32_e32 v15, v15
	v_pk_add_f32 v[8:9], v[8:9], 1.0 op_sel_hi:[1,0]
	v_pk_add_f32 v[10:11], v[10:11], 1.0 op_sel_hi:[1,0]
	v_pk_add_f32 v[12:13], v[12:13], 1.0 op_sel_hi:[1,0]
	v_pk_add_f32 v[14:15], v[14:15], 1.0 op_sel_hi:[1,0]
	v_rcp_f32_e32 v8, v8
	v_rcp_f32_e32 v9, v9
	v_rcp_f32_e32 v10, v10
	v_rcp_f32_e32 v11, v11
	v_rcp_f32_e32 v12, v12
	v_rcp_f32_e32 v13, v13
	v_rcp_f32_e32 v14, v14
	v_rcp_f32_e32 v15, v15
	v_med3_f32 v80, v80, s42, v205
	v_med3_f32 v81, v81, s42, v205
	v_med3_f32 v82, v82, s42, v205
	v_med3_f32 v83, v83, s42, v205
	v_med3_f32 v72, v72, s42, v205
	v_med3_f32 v73, v73, s42, v205
	v_med3_f32 v74, v74, s42, v205
	v_med3_f32 v75, v75, s42, v205
	v_pk_mul_f32 v[8:9], v[8:9], v[84:85]
	v_pk_mul_f32 v[10:11], v[10:11], v[86:87]
	v_pk_mul_f32 v[12:13], v[12:13], v[76:77]
	v_pk_mul_f32 v[14:15], v[14:15], v[78:79]
	v_pk_mul_f32 v[8:9], v[8:9], v[80:81]
	v_pk_mul_f32 v[10:11], v[10:11], v[82:83]
	v_pk_mul_f32 v[12:13], v[12:13], v[72:73]
	v_pk_mul_f32 v[14:15], v[14:15], v[74:75]
	v_cvt_pk_fp8_f32 v222, v8, v9
	v_cvt_pk_fp8_f32 v223, v12, v13
	v_cvt_pk_fp8_f32 v222, v10, v11 op_sel:[0,0,1]
	v_cvt_pk_fp8_f32 v223, v14, v15 op_sel:[0,0,1]
	s_nop 1
	v_permlane16_swap_b32_e32 v220, v222
	v_permlane16_swap_b32_e32 v221, v223
	global_store_dwordx4 v[16:17], v[220:223], off
	v_lshl_add_u64 v[16:17], v[16:17], 0, s[58:59]
	v_min_f32_e32 v36, s65, v36
	v_min_f32_e32 v37, s65, v37
	v_min_f32_e32 v38, s65, v38
	v_min_f32_e32 v39, s65, v39
	v_min_f32_e32 v28, s65, v28
	v_min_f32_e32 v29, s65, v29
	v_min_f32_e32 v30, s65, v30
	v_min_f32_e32 v31, s65, v31
	v_pk_mul_f32 v[0:1], v[36:37], s[62:63]
	v_pk_mul_f32 v[2:3], v[38:39], s[62:63]
	v_pk_mul_f32 v[4:5], v[28:29], s[62:63]
	v_pk_mul_f32 v[6:7], v[30:31], s[62:63]
	v_exp_f32_e32 v0, v0
	v_exp_f32_e32 v1, v1
	v_exp_f32_e32 v2, v2
	v_exp_f32_e32 v3, v3
	v_exp_f32_e32 v4, v4
	v_exp_f32_e32 v5, v5
	v_exp_f32_e32 v6, v6
	v_exp_f32_e32 v7, v7
	v_pk_add_f32 v[0:1], v[0:1], 1.0 op_sel_hi:[1,0]
	v_pk_add_f32 v[2:3], v[2:3], 1.0 op_sel_hi:[1,0]
	v_pk_add_f32 v[4:5], v[4:5], 1.0 op_sel_hi:[1,0]
	v_pk_add_f32 v[6:7], v[6:7], 1.0 op_sel_hi:[1,0]
	v_rcp_f32_e32 v0, v0
	v_rcp_f32_e32 v1, v1
	v_rcp_f32_e32 v2, v2
	v_rcp_f32_e32 v3, v3
	v_rcp_f32_e32 v4, v4
	v_rcp_f32_e32 v5, v5
	v_rcp_f32_e32 v6, v6
	v_rcp_f32_e32 v7, v7
	v_med3_f32 v32, v32, s42, v205
	v_med3_f32 v33, v33, s42, v205
	v_med3_f32 v34, v34, s42, v205
	v_med3_f32 v35, v35, s42, v205
	v_med3_f32 v24, v24, s42, v205
	v_med3_f32 v25, v25, s42, v205
	v_med3_f32 v26, v26, s42, v205
	v_med3_f32 v27, v27, s42, v205
	v_pk_mul_f32 v[0:1], v[0:1], v[36:37]
	v_pk_mul_f32 v[2:3], v[2:3], v[38:39]
	v_pk_mul_f32 v[4:5], v[4:5], v[28:29]
	v_pk_mul_f32 v[6:7], v[6:7], v[30:31]
	v_pk_mul_f32 v[0:1], v[0:1], v[32:33]
	v_pk_mul_f32 v[2:3], v[2:3], v[34:35]
	v_pk_mul_f32 v[4:5], v[4:5], v[24:25]
	v_pk_mul_f32 v[6:7], v[6:7], v[26:27]
	v_cvt_pk_fp8_f32 v224, v0, v1
	v_cvt_pk_fp8_f32 v225, v4, v5
	v_cvt_pk_fp8_f32 v224, v2, v3 op_sel:[0,0,1]
	v_cvt_pk_fp8_f32 v225, v6, v7 op_sel:[0,0,1]
	v_min_f32_e32 v52, s65, v52
	v_min_f32_e32 v53, s65, v53
	v_min_f32_e32 v54, s65, v54
	v_min_f32_e32 v55, s65, v55
	v_min_f32_e32 v44, s65, v44
	v_min_f32_e32 v45, s65, v45
	v_min_f32_e32 v46, s65, v46
	v_min_f32_e32 v47, s65, v47
	v_pk_mul_f32 v[8:9], v[52:53], s[62:63]
	v_pk_mul_f32 v[10:11], v[54:55], s[62:63]
	v_pk_mul_f32 v[12:13], v[44:45], s[62:63]
	v_pk_mul_f32 v[14:15], v[46:47], s[62:63]
	v_exp_f32_e32 v8, v8
	v_exp_f32_e32 v9, v9
	v_exp_f32_e32 v10, v10
	v_exp_f32_e32 v11, v11
	v_exp_f32_e32 v12, v12
	v_exp_f32_e32 v13, v13
	v_exp_f32_e32 v14, v14
	v_exp_f32_e32 v15, v15
	v_pk_add_f32 v[8:9], v[8:9], 1.0 op_sel_hi:[1,0]
	v_pk_add_f32 v[10:11], v[10:11], 1.0 op_sel_hi:[1,0]
	v_pk_add_f32 v[12:13], v[12:13], 1.0 op_sel_hi:[1,0]
	v_pk_add_f32 v[14:15], v[14:15], 1.0 op_sel_hi:[1,0]
	v_rcp_f32_e32 v8, v8
	v_rcp_f32_e32 v9, v9
	v_rcp_f32_e32 v10, v10
	v_rcp_f32_e32 v11, v11
	v_rcp_f32_e32 v12, v12
	v_rcp_f32_e32 v13, v13
	v_rcp_f32_e32 v14, v14
	v_rcp_f32_e32 v15, v15
	v_med3_f32 v48, v48, s42, v205
	v_med3_f32 v49, v49, s42, v205
	v_med3_f32 v50, v50, s42, v205
	v_med3_f32 v51, v51, s42, v205
	v_med3_f32 v40, v40, s42, v205
	v_med3_f32 v41, v41, s42, v205
	v_med3_f32 v42, v42, s42, v205
	v_med3_f32 v43, v43, s42, v205
	v_pk_mul_f32 v[8:9], v[8:9], v[52:53]
	v_pk_mul_f32 v[10:11], v[10:11], v[54:55]
	v_pk_mul_f32 v[12:13], v[12:13], v[44:45]
	v_pk_mul_f32 v[14:15], v[14:15], v[46:47]
	v_pk_mul_f32 v[8:9], v[8:9], v[48:49]
	v_pk_mul_f32 v[10:11], v[10:11], v[50:51]
	v_pk_mul_f32 v[12:13], v[12:13], v[40:41]
	v_pk_mul_f32 v[14:15], v[14:15], v[42:43]
	v_cvt_pk_fp8_f32 v226, v8, v9
	v_cvt_pk_fp8_f32 v227, v12, v13
	v_cvt_pk_fp8_f32 v226, v10, v11 op_sel:[0,0,1]
	v_cvt_pk_fp8_f32 v227, v14, v15 op_sel:[0,0,1]
	s_nop 1
	v_permlane16_swap_b32_e32 v224, v226
	v_permlane16_swap_b32_e32 v225, v227
	global_store_dwordx4 v[16:17], v[224:227], off
	s_mov_b32 s52, s49
	s_mov_b32 s51, s47
	s_mov_b32 s50, s48
	v_mov_b32_e32 v162, v160
	v_mov_b32_e32 v164, v158
	v_mov_b32_e32 v166, v207
	v_mov_b32_e32 v208, v206
	s_mov_b64 s[16:17], s[14:15]
	s_and_b64 vcc, exec, s[12:13]
	s_cbranch_vccnz .LBB0_1338

.LBB0_1334:
	s_add_u32 s16, s16, 0x100
	v_mov_b32_e32 v165, v157
	v_mov_b32_e32 v163, v157
	v_mov_b32_e32 v159, v157
	v_mov_b32_e32 v161, v157
	s_addc_u32 s17, s17, 0
	s_mov_b32 s53, -2
	s_mov_b64 s[18:19], s[8:9]
	v_lshl_add_u32 v16, s52, 10, v188
	ds_read_b128 v[0:3], v16
	ds_read_b128 v[4:7], v16 offset:16
	ds_read_b128 v[8:11], v16 offset:512
	ds_read_b128 v[12:15], v16 offset:528
	s_waitcnt lgkmcnt(0)
	v_fma_f32 v8, v8, 4.0, 4.0
	v_fma_f32 v9, v9, 4.0, 4.0
	v_fma_f32 v10, v10, 4.0, 4.0
	v_fma_f32 v11, v11, 4.0, 4.0
	v_fma_f32 v12, v12, 4.0, 4.0
	v_fma_f32 v13, v13, 4.0, 4.0
	v_fma_f32 v14, v14, 4.0, 4.0
	v_fma_f32 v15, v15, 4.0, 4.0
	v_mov_b64_e32 v[148:149], v[0:1]
	v_mov_b64_e32 v[144:145], v[8:9]
	v_mov_b64_e32 v[150:151], v[2:3]
	v_mov_b64_e32 v[146:147], v[10:11]
	v_mov_b64_e32 v[140:141], v[4:5]
	v_mov_b64_e32 v[136:137], v[12:13]
	v_mov_b64_e32 v[142:143], v[6:7]
	v_mov_b64_e32 v[138:139], v[14:15]
	v_mov_b64_e32 v[132:133], v[0:1]
	v_mov_b64_e32 v[128:129], v[8:9]
	v_mov_b64_e32 v[134:135], v[2:3]
	v_mov_b64_e32 v[130:131], v[10:11]
	v_mov_b64_e32 v[124:125], v[4:5]
	v_mov_b64_e32 v[120:121], v[12:13]
	v_mov_b64_e32 v[126:127], v[6:7]
	v_mov_b64_e32 v[122:123], v[14:15]
	v_mov_b64_e32 v[116:117], v[0:1]
	v_mov_b64_e32 v[112:113], v[8:9]
	v_mov_b64_e32 v[118:119], v[2:3]
	v_mov_b64_e32 v[114:115], v[10:11]
	v_mov_b64_e32 v[108:109], v[4:5]
	v_mov_b64_e32 v[104:105], v[12:13]
	v_mov_b64_e32 v[110:111], v[6:7]
	v_mov_b64_e32 v[106:107], v[14:15]
	v_mov_b64_e32 v[100:101], v[0:1]
	v_mov_b64_e32 v[96:97], v[8:9]
	v_mov_b64_e32 v[102:103], v[2:3]
	v_mov_b64_e32 v[98:99], v[10:11]
	v_mov_b64_e32 v[92:93], v[4:5]
	v_mov_b64_e32 v[88:89], v[12:13]
	v_mov_b64_e32 v[94:95], v[6:7]
	v_mov_b64_e32 v[90:91], v[14:15]
	v_mov_b64_e32 v[84:85], v[0:1]
	v_mov_b64_e32 v[80:81], v[8:9]
	v_mov_b64_e32 v[86:87], v[2:3]
	v_mov_b64_e32 v[82:83], v[10:11]
	v_mov_b64_e32 v[76:77], v[4:5]
	v_mov_b64_e32 v[72:73], v[12:13]
	v_mov_b64_e32 v[78:79], v[6:7]
	v_mov_b64_e32 v[74:75], v[14:15]
	v_mov_b64_e32 v[68:69], v[0:1]
	v_mov_b64_e32 v[64:65], v[8:9]
	v_mov_b64_e32 v[70:71], v[2:3]
	v_mov_b64_e32 v[66:67], v[10:11]
	v_mov_b64_e32 v[60:61], v[4:5]
	v_mov_b64_e32 v[56:57], v[12:13]
	v_mov_b64_e32 v[62:63], v[6:7]
	v_mov_b64_e32 v[58:59], v[14:15]
	v_mov_b64_e32 v[52:53], v[0:1]
	v_mov_b64_e32 v[48:49], v[8:9]
	v_mov_b64_e32 v[54:55], v[2:3]
	v_mov_b64_e32 v[50:51], v[10:11]
	v_mov_b64_e32 v[44:45], v[4:5]
	v_mov_b64_e32 v[40:41], v[12:13]
	v_mov_b64_e32 v[46:47], v[6:7]
	v_mov_b64_e32 v[42:43], v[14:15]
	v_mov_b64_e32 v[36:37], v[0:1]
	v_mov_b64_e32 v[32:33], v[8:9]
	v_mov_b64_e32 v[38:39], v[2:3]
	v_mov_b64_e32 v[34:35], v[10:11]
	v_mov_b64_e32 v[28:29], v[4:5]
	v_mov_b64_e32 v[24:25], v[12:13]
	v_mov_b64_e32 v[30:31], v[6:7]
	v_mov_b64_e32 v[26:27], v[14:15]
	s_branch .LBB0_1336

.LBB0_1418:
	s_ashr_i32 s9, s8, 31
	s_lshl_b64 s[14:15], s[8:9], 19
	s_add_u32 s14, s25, s14
	s_addc_u32 s15, s26, s15
	s_and_b64 s[22:23], s[22:23], exec
	s_cselect_b32 s9, s15, s19
	s_cselect_b32 s55, s14, s18
	s_add_u32 s18, s18, 0x80
	s_addc_u32 s19, s19, 0
	s_add_u32 s56, s20, 0x100
	s_addc_u32 s57, s21, 0
	s_mov_b32 s58, -2
	v_lshl_add_u32 v208, s17, 10, v174
	ds_read_b128 v[192:195], v208
	ds_read_b128 v[196:199], v208 offset:16
	ds_read_b128 v[200:203], v208 offset:512
	ds_read_b128 v[204:207], v208 offset:528
	s_mov_b32 s59, 0x41800000
	s_waitcnt lgkmcnt(0)
	v_mul_f32_e32 v192, s59, v192
	v_mul_f32_e32 v193, s59, v193
	v_mul_f32_e32 v194, s59, v194
	v_mul_f32_e32 v195, s59, v195
	v_mul_f32_e32 v196, s59, v196
	v_mul_f32_e32 v197, s59, v197
	v_mul_f32_e32 v198, s59, v198
	v_mul_f32_e32 v199, s59, v199
	v_mul_f32_e32 v200, s59, v200
	v_mul_f32_e32 v201, s59, v201
	v_mul_f32_e32 v202, s59, v202
	v_mul_f32_e32 v203, s59, v203
	v_mul_f32_e32 v204, s59, v204
	v_mul_f32_e32 v205, s59, v205
	v_mul_f32_e32 v206, s59, v206
	v_mul_f32_e32 v207, s59, v207
	v_mov_b64_e32 v[140:141], v[192:193]
	v_mov_b64_e32 v[142:143], v[194:195]
	v_mov_b64_e32 v[136:137], v[196:197]
	v_mov_b64_e32 v[138:139], v[198:199]
	v_mov_b64_e32 v[132:133], v[192:193]
	v_mov_b64_e32 v[134:135], v[194:195]
	v_mov_b64_e32 v[128:129], v[196:197]
	v_mov_b64_e32 v[130:131], v[198:199]
	v_mov_b64_e32 v[124:125], v[192:193]
	v_mov_b64_e32 v[126:127], v[194:195]
	v_mov_b64_e32 v[120:121], v[196:197]
	v_mov_b64_e32 v[122:123], v[198:199]
	v_mov_b64_e32 v[116:117], v[192:193]
	v_mov_b64_e32 v[118:119], v[194:195]
	v_mov_b64_e32 v[112:113], v[196:197]
	v_mov_b64_e32 v[114:115], v[198:199]
	v_mov_b64_e32 v[84:85], v[200:201]
	v_mov_b64_e32 v[86:87], v[202:203]
	v_mov_b64_e32 v[76:77], v[204:205]
	v_mov_b64_e32 v[78:79], v[206:207]
	v_mov_b64_e32 v[68:69], v[200:201]
	v_mov_b64_e32 v[70:71], v[202:203]
	v_mov_b64_e32 v[64:65], v[204:205]
	v_mov_b64_e32 v[66:67], v[206:207]
	v_mov_b64_e32 v[60:61], v[200:201]
	v_mov_b64_e32 v[62:63], v[202:203]
	v_mov_b64_e32 v[56:57], v[204:205]
	v_mov_b64_e32 v[58:59], v[206:207]
	v_mov_b64_e32 v[52:53], v[200:201]
	v_mov_b64_e32 v[54:55], v[202:203]
	v_mov_b64_e32 v[48:49], v[204:205]
	v_mov_b64_e32 v[50:51], v[206:207]
	v_mov_b64_e32 v[108:109], v[192:193]
	v_mov_b64_e32 v[110:111], v[194:195]
	v_mov_b64_e32 v[104:105], v[196:197]
	v_mov_b64_e32 v[106:107], v[198:199]
	v_mov_b64_e32 v[100:101], v[192:193]
	v_mov_b64_e32 v[102:103], v[194:195]
	v_mov_b64_e32 v[96:97], v[196:197]
	v_mov_b64_e32 v[98:99], v[198:199]
	v_mov_b64_e32 v[92:93], v[192:193]
	v_mov_b64_e32 v[94:95], v[194:195]
	v_mov_b64_e32 v[88:89], v[196:197]
	v_mov_b64_e32 v[90:91], v[198:199]
	v_mov_b64_e32 v[80:81], v[192:193]
	v_mov_b64_e32 v[82:83], v[194:195]
	v_mov_b64_e32 v[72:73], v[196:197]
	v_mov_b64_e32 v[74:75], v[198:199]
	v_mov_b64_e32 v[44:45], v[200:201]
	v_mov_b64_e32 v[46:47], v[202:203]
	v_mov_b64_e32 v[40:41], v[204:205]
	v_mov_b64_e32 v[42:43], v[206:207]
	v_mov_b64_e32 v[36:37], v[200:201]
	v_mov_b64_e32 v[38:39], v[202:203]
	v_mov_b64_e32 v[32:33], v[204:205]
	v_mov_b64_e32 v[34:35], v[206:207]
	v_mov_b64_e32 v[28:29], v[200:201]
	v_mov_b64_e32 v[30:31], v[202:203]
	v_mov_b64_e32 v[24:25], v[204:205]
	v_mov_b64_e32 v[26:27], v[206:207]
	v_mov_b64_e32 v[20:21], v[200:201]
	v_mov_b64_e32 v[22:23], v[202:203]
	v_mov_b64_e32 v[16:17], v[204:205]
	v_mov_b64_e32 v[18:19], v[206:207]
.LBB0_1419:
	ds_read_b128 v[0:3], v170
	ds_read_b128 v[4:7], v175
	ds_read_b128 v[8:11], v176
	ds_read_b128 v[12:15], v177
	s_add_u32 s20, s18, 0x80
	s_addc_u32 s21, s19, 0
	s_cmp_eq_u32 s58, 12
	s_cselect_b32 s23, s9, s21
	s_cselect_b32 s22, s55, s20
	s_cselect_b32 s21, s13, s57
	s_cselect_b32 s20, s12, s56
	v_lshl_add_u64 v[162:163], s[18:19], 0, v[160:161]
	s_add_i32 m0, s29, 0xc000
	ds_read_b128 v[192:195], v188
	ds_read_b128 v[196:199], v188 offset:1024
	ds_read_b128 v[200:203], v188 offset:2048
	ds_read_b128 v[204:207], v188 offset:3072
	ds_read_b128 v[208:211], v188 offset:4096
	ds_read_b128 v[212:215], v188 offset:5120
	ds_read_b128 v[216:219], v188 offset:6144
	ds_read_b128 v[220:223], v188 offset:7168
	global_load_lds_dwordx4 v[162:163], off
	v_lshl_add_u64 v[162:163], s[18:19], 0, v[158:159]
	s_add_i32 m0, s29, 0xe000
	s_nop 0
	global_load_lds_dwordx4 v[162:163], off
	s_waitcnt lgkmcnt(8)
	s_barrier
	s_waitcnt lgkmcnt(0)
	s_setprio 1
	s_waitcnt lgkmcnt(0)
	v_mfma_scale_f32_16x16x128_f8f6f4 v[140:143], v[0:7], v[192:199], v[140:143], v189, v190 op_sel_hi:[0,0,0]
	v_mfma_scale_f32_16x16x128_f8f6f4 v[136:139], v[8:15], v[192:199], v[136:139], v189, v190 op_sel_hi:[0,0,0]
	v_mfma_scale_f32_16x16x128_f8f6f4 v[132:135], v[0:7], v[200:207], v[132:135], v189, v190 op_sel_hi:[0,0,0]
	v_mfma_scale_f32_16x16x128_f8f6f4 v[128:131], v[8:15], v[200:207], v[128:131], v189, v190 op_sel_hi:[0,0,0]
	v_mfma_scale_f32_16x16x128_f8f6f4 v[124:127], v[0:7], v[208:215], v[124:127], v189, v190 op_sel_hi:[0,0,0]
	v_mfma_scale_f32_16x16x128_f8f6f4 v[120:123], v[8:15], v[208:215], v[120:123], v189, v190 op_sel_hi:[0,0,0]
	v_mfma_scale_f32_16x16x128_f8f6f4 v[116:119], v[0:7], v[216:223], v[116:119], v189, v190 op_sel_hi:[0,0,0]
	v_mfma_scale_f32_16x16x128_f8f6f4 v[112:115], v[8:15], v[216:223], v[112:115], v189, v190 op_sel_hi:[0,0,0]
	s_setprio 0
	s_barrier
	s_mov_b32 m0, s30
	v_lshl_add_u64 v[162:163], s[20:21], 0, v[146:147]
	ds_read_b128 v[224:227], v171
	ds_read_b128 v[228:231], v178
	ds_read_b128 v[232:235], v179
	ds_read_b128 v[236:239], v180
	global_load_lds_dwordx4 v[162:163], off
	v_lshl_add_u64 v[164:165], s[20:21], 0, v[144:145]
	s_mov_b32 m0, s31
	s_nop 0
	global_load_lds_dwordx4 v[164:165], off
	s_barrier
	s_waitcnt lgkmcnt(0)
	s_setprio 1
	s_waitcnt lgkmcnt(0)
	v_mfma_scale_f32_16x16x128_f8f6f4 v[84:87], v[224:231], v[192:199], v[84:87], v189, v190 op_sel_hi:[0,0,0]
	v_mfma_scale_f32_16x16x128_f8f6f4 v[76:79], v[232:239], v[192:199], v[76:79], v189, v190 op_sel_hi:[0,0,0]
	v_mfma_scale_f32_16x16x128_f8f6f4 v[68:71], v[224:231], v[200:207], v[68:71], v189, v190 op_sel_hi:[0,0,0]
	v_mfma_scale_f32_16x16x128_f8f6f4 v[64:67], v[232:239], v[200:207], v[64:67], v189, v190 op_sel_hi:[0,0,0]
	v_mfma_scale_f32_16x16x128_f8f6f4 v[60:63], v[224:231], v[208:215], v[60:63], v189, v190 op_sel_hi:[0,0,0]
	v_mfma_scale_f32_16x16x128_f8f6f4 v[56:59], v[232:239], v[208:215], v[56:59], v189, v190 op_sel_hi:[0,0,0]
	v_mfma_scale_f32_16x16x128_f8f6f4 v[52:55], v[224:231], v[216:223], v[52:55], v189, v190 op_sel_hi:[0,0,0]
	v_mfma_scale_f32_16x16x128_f8f6f4 v[48:51], v[232:239], v[216:223], v[48:51], v189, v190 op_sel_hi:[0,0,0]
	s_setprio 0
	s_mov_b32 m0, s29
	v_lshl_add_u64 v[166:167], s[22:23], 0, v[148:149]
	s_barrier
	ds_read_b128 v[192:195], v188 offset:16384
	ds_read_b128 v[196:199], v188 offset:17408
	ds_read_b128 v[200:203], v188 offset:18432
	ds_read_b128 v[204:207], v188 offset:19456
	ds_read_b128 v[208:211], v188 offset:20480
	ds_read_b128 v[212:215], v188 offset:21504
	ds_read_b128 v[216:219], v188 offset:22528
	ds_read_b128 v[220:223], v188 offset:23552
	global_load_lds_dwordx4 v[166:167], off
	v_lshl_add_u64 v[168:169], s[22:23], 0, v[150:151]
	s_mov_b32 m0, s33
	s_nop 0
	global_load_lds_dwordx4 v[168:169], off
	s_barrier
	s_waitcnt lgkmcnt(0)
	s_setprio 1
	s_waitcnt lgkmcnt(0)
	v_mfma_scale_f32_16x16x128_f8f6f4 v[108:111], v[0:7], v[192:199], v[108:111], v189, v190 op_sel_hi:[0,0,0]
	v_mfma_scale_f32_16x16x128_f8f6f4 v[104:107], v[8:15], v[192:199], v[104:107], v189, v190 op_sel_hi:[0,0,0]
	v_mfma_scale_f32_16x16x128_f8f6f4 v[100:103], v[0:7], v[200:207], v[100:103], v189, v190 op_sel_hi:[0,0,0]
	v_mfma_scale_f32_16x16x128_f8f6f4 v[96:99], v[8:15], v[200:207], v[96:99], v189, v190 op_sel_hi:[0,0,0]
	v_mfma_scale_f32_16x16x128_f8f6f4 v[92:95], v[0:7], v[208:215], v[92:95], v189, v190 op_sel_hi:[0,0,0]
	v_mfma_scale_f32_16x16x128_f8f6f4 v[88:91], v[8:15], v[208:215], v[88:91], v189, v190 op_sel_hi:[0,0,0]
	v_mfma_scale_f32_16x16x128_f8f6f4 v[80:83], v[0:7], v[216:223], v[80:83], v189, v190 op_sel_hi:[0,0,0]
	v_mfma_scale_f32_16x16x128_f8f6f4 v[72:75], v[8:15], v[216:223], v[72:75], v189, v190 op_sel_hi:[0,0,0]
	s_setprio 0
	s_barrier
	s_add_u32 s60, s20, 0x40000
	s_addc_u32 s61, s21, 0
	s_mov_b32 m0, s34
	v_lshl_add_u64 v[0:1], s[60:61], 0, v[146:147]
	global_load_lds_dwordx4 v[0:1], off
	v_lshl_add_u64 v[0:1], s[60:61], 0, v[144:145]
	s_mov_b32 m0, s35
	s_nop 0
	global_load_lds_dwordx4 v[0:1], off
	s_waitcnt vmcnt(6)
	s_barrier
	s_setprio 1
	v_mfma_scale_f32_16x16x128_f8f6f4 v[44:47], v[224:231], v[192:199], v[44:47], v189, v190 op_sel_hi:[0,0,0]
	v_mfma_scale_f32_16x16x128_f8f6f4 v[40:43], v[232:239], v[192:199], v[40:43], v189, v190 op_sel_hi:[0,0,0]
	v_mfma_scale_f32_16x16x128_f8f6f4 v[36:39], v[224:231], v[200:207], v[36:39], v189, v190 op_sel_hi:[0,0,0]
	v_mfma_scale_f32_16x16x128_f8f6f4 v[32:35], v[232:239], v[200:207], v[32:35], v189, v190 op_sel_hi:[0,0,0]
	v_mfma_scale_f32_16x16x128_f8f6f4 v[28:31], v[224:231], v[208:215], v[28:31], v189, v190 op_sel_hi:[0,0,0]
	v_mfma_scale_f32_16x16x128_f8f6f4 v[24:27], v[232:239], v[208:215], v[24:27], v189, v190 op_sel_hi:[0,0,0]
	v_mfma_scale_f32_16x16x128_f8f6f4 v[20:23], v[224:231], v[216:223], v[20:23], v189, v190 op_sel_hi:[0,0,0]
	v_mfma_scale_f32_16x16x128_f8f6f4 v[16:19], v[232:239], v[216:223], v[16:19], v189, v190 op_sel_hi:[0,0,0]
	s_setprio 0
	s_barrier
	ds_read_b128 v[0:3], v172
	ds_read_b128 v[4:7], v181
	ds_read_b128 v[8:11], v182
	ds_read_b128 v[12:15], v183
	s_mov_b32 m0, s36
	v_lshl_add_u64 v[224:225], s[22:23], 0, v[152:153]
	ds_read_b128 v[192:195], v188 offset:32768
	ds_read_b128 v[196:199], v188 offset:33792
	ds_read_b128 v[200:203], v188 offset:34816
	ds_read_b128 v[204:207], v188 offset:35840
	ds_read_b128 v[208:211], v188 offset:36864
	ds_read_b128 v[212:215], v188 offset:37888
	ds_read_b128 v[216:219], v188 offset:38912
	ds_read_b128 v[220:223], v188 offset:39936
	global_load_lds_dwordx4 v[224:225], off
	v_lshl_add_u64 v[224:225], s[22:23], 0, v[154:155]
	s_mov_b32 m0, s37
	s_nop 0
	global_load_lds_dwordx4 v[224:225], off
	s_waitcnt lgkmcnt(8)
	s_barrier
	s_waitcnt lgkmcnt(0)
	s_setprio 1
	s_waitcnt lgkmcnt(0)
	v_mfma_scale_f32_16x16x128_f8f6f4 v[140:143], v[0:7], v[192:199], v[140:143], v189, v190 op_sel_hi:[0,0,0]
	v_mfma_scale_f32_16x16x128_f8f6f4 v[136:139], v[8:15], v[192:199], v[136:139], v189, v190 op_sel_hi:[0,0,0]
	v_mfma_scale_f32_16x16x128_f8f6f4 v[132:135], v[0:7], v[200:207], v[132:135], v189, v190 op_sel_hi:[0,0,0]
	v_mfma_scale_f32_16x16x128_f8f6f4 v[128:131], v[8:15], v[200:207], v[128:131], v189, v190 op_sel_hi:[0,0,0]
	v_mfma_scale_f32_16x16x128_f8f6f4 v[124:127], v[0:7], v[208:215], v[124:127], v189, v190 op_sel_hi:[0,0,0]
	v_mfma_scale_f32_16x16x128_f8f6f4 v[120:123], v[8:15], v[208:215], v[120:123], v189, v190 op_sel_hi:[0,0,0]
	v_mfma_scale_f32_16x16x128_f8f6f4 v[116:119], v[0:7], v[216:223], v[116:119], v189, v190 op_sel_hi:[0,0,0]
	v_mfma_scale_f32_16x16x128_f8f6f4 v[112:115], v[8:15], v[216:223], v[112:115], v189, v190 op_sel_hi:[0,0,0]
	s_setprio 0
	s_barrier
	s_mov_b32 m0, s40
	v_lshl_add_u64 v[162:163], v[162:163], 0, s[4:5]
	ds_read_b128 v[224:227], v173
	ds_read_b128 v[228:231], v184
	ds_read_b128 v[232:235], v185
	ds_read_b128 v[236:239], v186
	global_load_lds_dwordx4 v[162:163], off
	v_lshl_add_u64 v[162:163], v[164:165], 0, s[4:5]
	s_mov_b32 m0, s41
	s_nop 0
	global_load_lds_dwordx4 v[162:163], off
	s_barrier
	s_waitcnt lgkmcnt(0)
	s_setprio 1
	s_waitcnt lgkmcnt(0)
	v_mfma_scale_f32_16x16x128_f8f6f4 v[84:87], v[224:231], v[192:199], v[84:87], v189, v190 op_sel_hi:[0,0,0]
	v_mfma_scale_f32_16x16x128_f8f6f4 v[76:79], v[232:239], v[192:199], v[76:79], v189, v190 op_sel_hi:[0,0,0]
	v_mfma_scale_f32_16x16x128_f8f6f4 v[68:71], v[224:231], v[200:207], v[68:71], v189, v190 op_sel_hi:[0,0,0]
	v_mfma_scale_f32_16x16x128_f8f6f4 v[64:67], v[232:239], v[200:207], v[64:67], v189, v190 op_sel_hi:[0,0,0]
	v_mfma_scale_f32_16x16x128_f8f6f4 v[60:63], v[224:231], v[208:215], v[60:63], v189, v190 op_sel_hi:[0,0,0]
	v_mfma_scale_f32_16x16x128_f8f6f4 v[56:59], v[232:239], v[208:215], v[56:59], v189, v190 op_sel_hi:[0,0,0]
	v_mfma_scale_f32_16x16x128_f8f6f4 v[52:55], v[224:231], v[216:223], v[52:55], v189, v190 op_sel_hi:[0,0,0]
	v_mfma_scale_f32_16x16x128_f8f6f4 v[48:51], v[232:239], v[216:223], v[48:51], v189, v190 op_sel_hi:[0,0,0]
	s_setprio 0
	s_mov_b32 m0, s42
	v_lshl_add_u64 v[162:163], v[166:167], 0, s[4:5]
	s_barrier
	ds_read_b128 v[192:195], v188 offset:49152
	ds_read_b128 v[196:199], v188 offset:50176
	ds_read_b128 v[200:203], v188 offset:51200
	ds_read_b128 v[204:207], v188 offset:52224
	ds_read_b128 v[208:211], v188 offset:53248
	ds_read_b128 v[212:215], v188 offset:54272
	ds_read_b128 v[216:219], v188 offset:55296
	ds_read_b128 v[220:223], v188 offset:56320
	global_load_lds_dwordx4 v[162:163], off
	v_lshl_add_u64 v[162:163], v[168:169], 0, s[4:5]
	s_mov_b32 m0, s43
	s_nop 0
	global_load_lds_dwordx4 v[162:163], off
	s_barrier
	s_waitcnt lgkmcnt(0)
	s_setprio 1
	s_waitcnt lgkmcnt(0)
	v_mfma_scale_f32_16x16x128_f8f6f4 v[108:111], v[0:7], v[192:199], v[108:111], v189, v190 op_sel_hi:[0,0,0]
	v_mfma_scale_f32_16x16x128_f8f6f4 v[104:107], v[8:15], v[192:199], v[104:107], v189, v190 op_sel_hi:[0,0,0]
	v_mfma_scale_f32_16x16x128_f8f6f4 v[100:103], v[0:7], v[200:207], v[100:103], v189, v190 op_sel_hi:[0,0,0]
	v_mfma_scale_f32_16x16x128_f8f6f4 v[96:99], v[8:15], v[200:207], v[96:99], v189, v190 op_sel_hi:[0,0,0]
	v_mfma_scale_f32_16x16x128_f8f6f4 v[92:95], v[0:7], v[208:215], v[92:95], v189, v190 op_sel_hi:[0,0,0]
	v_mfma_scale_f32_16x16x128_f8f6f4 v[88:91], v[8:15], v[208:215], v[88:91], v189, v190 op_sel_hi:[0,0,0]
	v_mfma_scale_f32_16x16x128_f8f6f4 v[80:83], v[0:7], v[216:223], v[80:83], v189, v190 op_sel_hi:[0,0,0]
	v_mfma_scale_f32_16x16x128_f8f6f4 v[72:75], v[8:15], v[216:223], v[72:75], v189, v190 op_sel_hi:[0,0,0]
	s_setprio 0
	s_barrier
	s_add_u32 s20, s20, 0x40080
	s_addc_u32 s21, s21, 0
	s_mov_b32 m0, s44
	v_lshl_add_u64 v[0:1], s[20:21], 0, v[146:147]
	global_load_lds_dwordx4 v[0:1], off
	v_lshl_add_u64 v[0:1], s[20:21], 0, v[144:145]
	s_mov_b32 m0, s45
	s_nop 0
	global_load_lds_dwordx4 v[0:1], off
	s_waitcnt vmcnt(6)
	s_barrier
	s_setprio 1
	v_mfma_scale_f32_16x16x128_f8f6f4 v[44:47], v[224:231], v[192:199], v[44:47], v189, v190 op_sel_hi:[0,0,0]
	v_mfma_scale_f32_16x16x128_f8f6f4 v[40:43], v[232:239], v[192:199], v[40:43], v189, v190 op_sel_hi:[0,0,0]
	v_mfma_scale_f32_16x16x128_f8f6f4 v[36:39], v[224:231], v[200:207], v[36:39], v189, v190 op_sel_hi:[0,0,0]
	v_mfma_scale_f32_16x16x128_f8f6f4 v[32:35], v[232:239], v[200:207], v[32:35], v189, v190 op_sel_hi:[0,0,0]
	v_mfma_scale_f32_16x16x128_f8f6f4 v[28:31], v[224:231], v[208:215], v[28:31], v189, v190 op_sel_hi:[0,0,0]
	v_mfma_scale_f32_16x16x128_f8f6f4 v[24:27], v[232:239], v[208:215], v[24:27], v189, v190 op_sel_hi:[0,0,0]
	v_mfma_scale_f32_16x16x128_f8f6f4 v[20:23], v[224:231], v[216:223], v[20:23], v189, v190 op_sel_hi:[0,0,0]
	v_mfma_scale_f32_16x16x128_f8f6f4 v[16:19], v[232:239], v[216:223], v[16:19], v189, v190 op_sel_hi:[0,0,0]
	s_setprio 0
	s_add_i32 s58, s58, 2
	s_add_u32 s18, s18, 0x100
	s_addc_u32 s19, s19, 0
	s_add_u32 s56, s56, 0x100
	s_addc_u32 s57, s57, 0
	s_cmp_gt_u32 s58, 13
	s_barrier
	s_cbranch_scc0 .LBB0_1419
	v_lshl_or_b32 v8, s54, 8, v187
	s_ashr_i32 s17, s16, 31
	s_lshl_b64 s[16:17], s[16:17], 19
	v_lshl_add_u64 v[10:11], v[156:157], 0, s[16:17]
	v_ashrrev_i32_e32 v9, 31, v8
	v_lshl_add_u64 v[8:9], v[10:11], 0, v[8:9]
	v_mbcnt_lo_u32_b32 v10, -1, 0
	v_mbcnt_hi_u32_b32 v10, -1, v10
	v_and_b32_e32 v10, 16, v10
	v_mov_b32_e32 v12, 0x8000
	v_cmp_eq_u32_e32 vcc, 0, v10
	s_nop 1
	v_cndmask_b32_e32 v12, -8, v12, vcc
	v_ashrrev_i32_e32 v13, 31, v12
	v_lshl_add_u64 v[8:9], v[8:9], 0, v[12:13]
	v_med3_f32 v132, v132, s7, v191
	v_med3_f32 v133, v133, s7, v191
	v_med3_f32 v134, v134, s7, v191
	v_med3_f32 v135, v135, s7, v191
	v_med3_f32 v128, v128, s7, v191
	v_med3_f32 v129, v129, s7, v191
	v_med3_f32 v130, v130, s7, v191
	v_med3_f32 v131, v131, s7, v191
	v_cvt_pk_fp8_f32 v224, v132, v133
	v_cvt_pk_fp8_f32 v225, v128, v129
	v_cvt_pk_fp8_f32 v224, v134, v135 op_sel:[0,0,1]
	v_cvt_pk_fp8_f32 v225, v130, v131 op_sel:[0,0,1]
	v_med3_f32 v140, v140, s7, v191
	v_med3_f32 v141, v141, s7, v191
	v_med3_f32 v142, v142, s7, v191
	v_med3_f32 v143, v143, s7, v191
	v_med3_f32 v136, v136, s7, v191
	v_med3_f32 v137, v137, s7, v191
	v_med3_f32 v138, v138, s7, v191
	v_med3_f32 v139, v139, s7, v191
	v_cvt_pk_fp8_f32 v226, v140, v141
	v_cvt_pk_fp8_f32 v227, v136, v137
	v_cvt_pk_fp8_f32 v226, v142, v143 op_sel:[0,0,1]
	v_cvt_pk_fp8_f32 v227, v138, v139 op_sel:[0,0,1]
	s_nop 1
	v_permlane16_swap_b32_e32 v224, v226
	v_permlane16_swap_b32_e32 v225, v227
	global_store_dwordx4 v[8:9], v[224:227], off
	v_med3_f32 v68, v68, s7, v191
	v_med3_f32 v69, v69, s7, v191
	v_med3_f32 v70, v70, s7, v191
	v_med3_f32 v71, v71, s7, v191
	v_med3_f32 v64, v64, s7, v191
	v_med3_f32 v65, v65, s7, v191
	v_med3_f32 v66, v66, s7, v191
	v_med3_f32 v67, v67, s7, v191
	v_cvt_pk_fp8_f32 v228, v68, v69
	v_cvt_pk_fp8_f32 v229, v64, v65
	v_cvt_pk_fp8_f32 v228, v70, v71 op_sel:[0,0,1]
	v_cvt_pk_fp8_f32 v229, v66, v67 op_sel:[0,0,1]
	v_med3_f32 v84, v84, s7, v191
	v_med3_f32 v85, v85, s7, v191
	v_med3_f32 v86, v86, s7, v191
	v_med3_f32 v87, v87, s7, v191
	v_med3_f32 v76, v76, s7, v191
	v_med3_f32 v77, v77, s7, v191
	v_med3_f32 v78, v78, s7, v191
	v_med3_f32 v79, v79, s7, v191
	v_cvt_pk_fp8_f32 v230, v84, v85
	v_cvt_pk_fp8_f32 v231, v76, v77
	v_cvt_pk_fp8_f32 v230, v86, v87 op_sel:[0,0,1]
	v_cvt_pk_fp8_f32 v231, v78, v79 op_sel:[0,0,1]
	s_nop 1
	v_permlane16_swap_b32_e32 v228, v230
	v_permlane16_swap_b32_e32 v229, v231
	global_store_dwordx4 v[8:9], v[228:231], off offset:128
	v_lshl_add_u64 v[8:9], v[8:9], 0, s[62:63]
	v_med3_f32 v116, v116, s7, v191
	v_med3_f32 v117, v117, s7, v191
	v_med3_f32 v118, v118, s7, v191
	v_med3_f32 v119, v119, s7, v191
	v_med3_f32 v112, v112, s7, v191
	v_med3_f32 v113, v113, s7, v191
	v_med3_f32 v114, v114, s7, v191
	v_med3_f32 v115, v115, s7, v191
	v_cvt_pk_fp8_f32 v232, v116, v117
	v_cvt_pk_fp8_f32 v233, v112, v113
	v_cvt_pk_fp8_f32 v232, v118, v119 op_sel:[0,0,1]
	v_cvt_pk_fp8_f32 v233, v114, v115 op_sel:[0,0,1]
	v_med3_f32 v124, v124, s7, v191
	v_med3_f32 v125, v125, s7, v191
	v_med3_f32 v126, v126, s7, v191
	v_med3_f32 v127, v127, s7, v191
	v_med3_f32 v120, v120, s7, v191
	v_med3_f32 v121, v121, s7, v191
	v_med3_f32 v122, v122, s7, v191
	v_med3_f32 v123, v123, s7, v191
	v_cvt_pk_fp8_f32 v234, v124, v125
	v_cvt_pk_fp8_f32 v235, v120, v121
	v_cvt_pk_fp8_f32 v234, v126, v127 op_sel:[0,0,1]
	v_cvt_pk_fp8_f32 v235, v122, v123 op_sel:[0,0,1]
	s_nop 1
	v_permlane16_swap_b32_e32 v232, v234
	v_permlane16_swap_b32_e32 v233, v235
	global_store_dwordx4 v[8:9], v[232:235], off
	v_med3_f32 v52, v52, s7, v191
	v_med3_f32 v53, v53, s7, v191
	v_med3_f32 v54, v54, s7, v191
	v_med3_f32 v55, v55, s7, v191
	v_med3_f32 v48, v48, s7, v191
	v_med3_f32 v49, v49, s7, v191
	v_med3_f32 v50, v50, s7, v191
	v_med3_f32 v51, v51, s7, v191
	v_cvt_pk_fp8_f32 v236, v52, v53
	v_cvt_pk_fp8_f32 v237, v48, v49
	v_cvt_pk_fp8_f32 v236, v54, v55 op_sel:[0,0,1]
	v_cvt_pk_fp8_f32 v237, v50, v51 op_sel:[0,0,1]
	v_med3_f32 v60, v60, s7, v191
	v_med3_f32 v61, v61, s7, v191
	v_med3_f32 v62, v62, s7, v191
	v_med3_f32 v63, v63, s7, v191
	v_med3_f32 v56, v56, s7, v191
	v_med3_f32 v57, v57, s7, v191
	v_med3_f32 v58, v58, s7, v191
	v_med3_f32 v59, v59, s7, v191
	v_cvt_pk_fp8_f32 v238, v60, v61
	v_cvt_pk_fp8_f32 v239, v56, v57
	v_cvt_pk_fp8_f32 v238, v62, v63 op_sel:[0,0,1]
	v_cvt_pk_fp8_f32 v239, v58, v59 op_sel:[0,0,1]
	s_nop 1
	v_permlane16_swap_b32_e32 v236, v238
	v_permlane16_swap_b32_e32 v237, v239
	global_store_dwordx4 v[8:9], v[236:239], off offset:128
	v_lshl_add_u64 v[8:9], v[8:9], 0, s[64:65]
	v_med3_f32 v100, v100, s7, v191
	v_med3_f32 v101, v101, s7, v191
	v_med3_f32 v102, v102, s7, v191
	v_med3_f32 v103, v103, s7, v191
	v_med3_f32 v96, v96, s7, v191
	v_med3_f32 v97, v97, s7, v191
	v_med3_f32 v98, v98, s7, v191
	v_med3_f32 v99, v99, s7, v191
	v_cvt_pk_fp8_f32 v224, v100, v101
	v_cvt_pk_fp8_f32 v225, v96, v97
	v_cvt_pk_fp8_f32 v224, v102, v103 op_sel:[0,0,1]
	v_cvt_pk_fp8_f32 v225, v98, v99 op_sel:[0,0,1]
	v_med3_f32 v108, v108, s7, v191
	v_med3_f32 v109, v109, s7, v191
	v_med3_f32 v110, v110, s7, v191
	v_med3_f32 v111, v111, s7, v191
	v_med3_f32 v104, v104, s7, v191
	v_med3_f32 v105, v105, s7, v191
	v_med3_f32 v106, v106, s7, v191
	v_med3_f32 v107, v107, s7, v191
	v_cvt_pk_fp8_f32 v226, v108, v109
	v_cvt_pk_fp8_f32 v227, v104, v105
	v_cvt_pk_fp8_f32 v226, v110, v111 op_sel:[0,0,1]
	v_cvt_pk_fp8_f32 v227, v106, v107 op_sel:[0,0,1]
	s_nop 1
	v_permlane16_swap_b32_e32 v224, v226
	v_permlane16_swap_b32_e32 v225, v227
	global_store_dwordx4 v[8:9], v[224:227], off
	v_med3_f32 v36, v36, s7, v191
	v_med3_f32 v37, v37, s7, v191
	v_med3_f32 v38, v38, s7, v191
	v_med3_f32 v39, v39, s7, v191
	v_med3_f32 v32, v32, s7, v191
	v_med3_f32 v33, v33, s7, v191
	v_med3_f32 v34, v34, s7, v191
	v_med3_f32 v35, v35, s7, v191
	v_cvt_pk_fp8_f32 v228, v36, v37
	v_cvt_pk_fp8_f32 v229, v32, v33
	v_cvt_pk_fp8_f32 v228, v38, v39 op_sel:[0,0,1]
	v_cvt_pk_fp8_f32 v229, v34, v35 op_sel:[0,0,1]
	v_med3_f32 v44, v44, s7, v191
	v_med3_f32 v45, v45, s7, v191
	v_med3_f32 v46, v46, s7, v191
	v_med3_f32 v47, v47, s7, v191
	v_med3_f32 v40, v40, s7, v191
	v_med3_f32 v41, v41, s7, v191
	v_med3_f32 v42, v42, s7, v191
	v_med3_f32 v43, v43, s7, v191
	v_cvt_pk_fp8_f32 v230, v44, v45
	v_cvt_pk_fp8_f32 v231, v40, v41
	v_cvt_pk_fp8_f32 v230, v46, v47 op_sel:[0,0,1]
	v_cvt_pk_fp8_f32 v231, v42, v43 op_sel:[0,0,1]
	s_nop 1
	v_permlane16_swap_b32_e32 v228, v230
	v_permlane16_swap_b32_e32 v229, v231
	global_store_dwordx4 v[8:9], v[228:231], off offset:128
	v_lshl_add_u64 v[8:9], v[8:9], 0, s[62:63]
	v_med3_f32 v80, v80, s7, v191
	v_med3_f32 v81, v81, s7, v191
	v_med3_f32 v82, v82, s7, v191
	v_med3_f32 v83, v83, s7, v191
	v_med3_f32 v72, v72, s7, v191
	v_med3_f32 v73, v73, s7, v191
	v_med3_f32 v74, v74, s7, v191
	v_med3_f32 v75, v75, s7, v191
	v_cvt_pk_fp8_f32 v232, v80, v81
	v_cvt_pk_fp8_f32 v233, v72, v73
	v_cvt_pk_fp8_f32 v232, v82, v83 op_sel:[0,0,1]
	v_cvt_pk_fp8_f32 v233, v74, v75 op_sel:[0,0,1]
	v_med3_f32 v92, v92, s7, v191
	v_med3_f32 v93, v93, s7, v191
	v_med3_f32 v94, v94, s7, v191
	v_med3_f32 v95, v95, s7, v191
	v_med3_f32 v88, v88, s7, v191
	v_med3_f32 v89, v89, s7, v191
	v_med3_f32 v90, v90, s7, v191
	v_med3_f32 v91, v91, s7, v191
	v_cvt_pk_fp8_f32 v234, v92, v93
	v_cvt_pk_fp8_f32 v235, v88, v89
	v_cvt_pk_fp8_f32 v234, v94, v95 op_sel:[0,0,1]
	v_cvt_pk_fp8_f32 v235, v90, v91 op_sel:[0,0,1]
	s_nop 1
	v_permlane16_swap_b32_e32 v232, v234
	v_permlane16_swap_b32_e32 v233, v235
	global_store_dwordx4 v[8:9], v[232:235], off
	v_med3_f32 v20, v20, s7, v191
	v_med3_f32 v21, v21, s7, v191
	v_med3_f32 v22, v22, s7, v191
	v_med3_f32 v23, v23, s7, v191
	v_med3_f32 v16, v16, s7, v191
	v_med3_f32 v17, v17, s7, v191
	v_med3_f32 v18, v18, s7, v191
	v_med3_f32 v19, v19, s7, v191
	v_cvt_pk_fp8_f32 v236, v20, v21
	v_cvt_pk_fp8_f32 v237, v16, v17
	v_cvt_pk_fp8_f32 v236, v22, v23 op_sel:[0,0,1]
	v_cvt_pk_fp8_f32 v237, v18, v19 op_sel:[0,0,1]
	v_med3_f32 v28, v28, s7, v191
	v_med3_f32 v29, v29, s7, v191
	v_med3_f32 v30, v30, s7, v191
	v_med3_f32 v31, v31, s7, v191
	v_med3_f32 v24, v24, s7, v191
	v_med3_f32 v25, v25, s7, v191
	v_med3_f32 v26, v26, s7, v191
	v_med3_f32 v27, v27, s7, v191
	v_cvt_pk_fp8_f32 v238, v28, v29
	v_cvt_pk_fp8_f32 v239, v24, v25
	v_cvt_pk_fp8_f32 v238, v30, v31 op_sel:[0,0,1]
	v_cvt_pk_fp8_f32 v239, v26, v27 op_sel:[0,0,1]
	s_nop 1
	v_permlane16_swap_b32_e32 v236, v238
	v_permlane16_swap_b32_e32 v237, v239
	global_store_dwordx4 v[8:9], v[236:239], off offset:128
	s_and_b64 vcc, exec, s[10:11]
	s_mov_b32 s17, s53
	s_mov_b32 s54, s52
	s_mov_b32 s16, s8
	s_mov_b64 s[20:21], s[12:13]
	s_mov_b64 s[18:19], s[14:15]
	s_cbranch_vccz .LBB0_1413
	s_waitcnt vmcnt(0)
	s_cmpk_gt_u32 s24, 0xff
	s_cbranch_scc1 .LBB0_1423
	s_barrier
